# g10: g9 + fp8 GEMMs first K-tile: inline 0 as MFMA C operand instead of 64 v_mov_b64 zeroing inside the MFMA segments
# speedup vs baseline: 1.0137x; 1.0013x over previous
.LBB0_610:
	ds_read_b128 v[2:5], v188
	ds_read_b128 v[10:13], v188 offset:2048
	ds_read_b128 v[6:9], v189
	ds_read_b128 v[14:17], v189 offset:2048
	ds_read_b128 v[18:21], v190
	ds_read_b128 v[26:29], v190 offset:2048
	ds_read_b128 v[22:25], v191
	ds_read_b128 v[30:33], v191 offset:2048
	s_ashr_i32 s35, s34, 31
	s_lshl_b64 s[6:7], s[34:35], 19
	s_add_u32 s36, s46, s6
	s_addc_u32 s37, s47, s7
	s_and_b64 s[4:5], s[4:5], exec
	s_cselect_b32 s35, s37, s41
	s_cselect_b32 s66, s36, s40
	s_add_i32 s67, s39, 0xc000
	s_mov_b32 m0, s67
	s_add_i32 s68, s39, 0xe000
	ds_read_b128 v[38:41], v192
	ds_read_b128 v[42:45], v192 offset:1024
	ds_read_b128 v[46:49], v192 offset:2048
	ds_read_b128 v[50:53], v192 offset:3072
	ds_read_b128 v[54:57], v192 offset:4096
	ds_read_b128 v[58:61], v192 offset:5120
	ds_read_b128 v[62:65], v192 offset:6144
	ds_read_b128 v[66:69], v192 offset:7168
	global_load_lds_dwordx4 v172, s[18:19]
	s_mov_b32 m0, s68
	v_mov_b32_e32 v173, v169
	global_load_lds_dwordx4 v174, s[18:19]
	s_waitcnt vmcnt(8)
	s_waitcnt lgkmcnt(0)
	v_mov_b32_e32 v175, v169
	s_barrier
	s_setprio 1
	s_mov_b32 s4, 0
	s_mov_b32 s6, s4
	s_mov_b32 s7, s4
	s_mov_b32 s5, s4
	s_waitcnt lgkmcnt(0)
	v_mfma_scale_f32_16x16x128_f8f6f4 v[158:161], v[2:9], v[38:45], 0, v193, v194 op_sel_hi:[0,0,0]
	v_mfma_scale_f32_16x16x128_f8f6f4 v[154:157], v[10:17], v[38:45], 0, v193, v194 op_sel_hi:[0,0,0]
	v_mfma_scale_f32_16x16x128_f8f6f4 v[142:145], v[2:9], v[46:53], 0, v193, v194 op_sel_hi:[0,0,0]
	v_mfma_scale_f32_16x16x128_f8f6f4 v[138:141], v[10:17], v[46:53], 0, v193, v194 op_sel_hi:[0,0,0]
	v_mfma_scale_f32_16x16x128_f8f6f4 v[126:129], v[2:9], v[54:61], 0, v193, v194 op_sel_hi:[0,0,0]
	v_mfma_scale_f32_16x16x128_f8f6f4 v[122:125], v[10:17], v[54:61], 0, v193, v194 op_sel_hi:[0,0,0]
	v_mfma_scale_f32_16x16x128_f8f6f4 v[110:113], v[2:9], v[62:69], 0, v193, v194 op_sel_hi:[0,0,0]
	v_mfma_scale_f32_16x16x128_f8f6f4 v[106:109], v[10:17], v[62:69], 0, v193, v194 op_sel_hi:[0,0,0]
	s_setprio 0
	s_setprio 1
	v_mfma_scale_f32_16x16x128_f8f6f4 v[150:153], v[18:25], v[38:45], 0, v193, v194 op_sel_hi:[0,0,0]
	v_mfma_scale_f32_16x16x128_f8f6f4 v[146:149], v[26:33], v[38:45], 0, v193, v194 op_sel_hi:[0,0,0]
	v_mfma_scale_f32_16x16x128_f8f6f4 v[134:137], v[18:25], v[46:53], 0, v193, v194 op_sel_hi:[0,0,0]
	v_mfma_scale_f32_16x16x128_f8f6f4 v[130:133], v[26:33], v[46:53], 0, v193, v194 op_sel_hi:[0,0,0]
	v_mfma_scale_f32_16x16x128_f8f6f4 v[118:121], v[18:25], v[54:61], 0, v193, v194 op_sel_hi:[0,0,0]
	v_mfma_scale_f32_16x16x128_f8f6f4 v[114:117], v[26:33], v[54:61], 0, v193, v194 op_sel_hi:[0,0,0]
	v_mfma_scale_f32_16x16x128_f8f6f4 v[98:101], v[18:25], v[62:69], 0, v193, v194 op_sel_hi:[0,0,0]
	v_mfma_scale_f32_16x16x128_f8f6f4 v[90:93], v[26:33], v[62:69], 0, v193, v194 op_sel_hi:[0,0,0]
	s_setprio 0
	s_barrier
	s_add_i32 s5, s56, s48
	v_lshl_add_u64 v[176:177], s[40:41], 0, v[166:167]
	s_add_i32 s69, s5, 0x2000
	v_lshl_add_u64 v[38:39], v[176:177], 0, s[28:29]
	s_mov_b32 m0, s5
	v_lshl_add_u64 v[178:179], s[40:41], 0, v[164:165]
	s_add_u32 s6, s40, 0x4100
	ds_read_b128 v[50:53], v192 offset:16384
	ds_read_b128 v[54:57], v192 offset:17408
	ds_read_b128 v[202:205], v192 offset:18432
	ds_read_b128 v[206:209], v192 offset:19456
	ds_read_b128 v[210:213], v192 offset:20480
	ds_read_b128 v[214:217], v192 offset:21504
	ds_read_b128 v[218:221], v192 offset:22528
	ds_read_b128 v[222:225], v192 offset:23552
	global_load_lds_dwordx4 v[38:39], off
	v_lshl_add_u64 v[38:39], v[178:179], 0, s[28:29]
	s_mov_b32 m0, s69
	s_addc_u32 s7, s41, 0
	s_add_i32 s70, s57, s48
	global_load_lds_dwordx4 v[38:39], off
	v_lshl_add_u64 v[38:39], s[6:7], 0, v[166:167]
	s_mov_b32 m0, s70
	s_add_i32 s71, s70, 0x2000
	global_load_lds_dwordx4 v[38:39], off
	v_lshl_add_u64 v[38:39], s[6:7], 0, v[164:165]
	s_mov_b32 m0, s71
	s_nop 0
	global_load_lds_dwordx4 v[38:39], off
	s_mov_b32 m0, s39
	s_nop 0
	global_load_lds_dwordx4 v200, s[24:25]
	s_mov_b32 m0, s51
	s_nop 0
	global_load_lds_dwordx4 v170, s[24:25]
	s_waitcnt vmcnt(8)
	s_waitcnt lgkmcnt(0)
	s_barrier
	s_setprio 1
	s_waitcnt lgkmcnt(0)
	v_mfma_scale_f32_16x16x128_f8f6f4 v[102:105], v[2:9], v[50:57], 0, v193, v194 op_sel_hi:[0,0,0]
	v_mfma_scale_f32_16x16x128_f8f6f4 v[94:97], v[10:17], v[50:57], 0, v193, v194 op_sel_hi:[0,0,0]
	v_mfma_scale_f32_16x16x128_f8f6f4 v[78:81], v[2:9], v[202:209], 0, v193, v194 op_sel_hi:[0,0,0]
	v_mfma_scale_f32_16x16x128_f8f6f4 v[74:77], v[10:17], v[202:209], 0, v193, v194 op_sel_hi:[0,0,0]
	v_mfma_scale_f32_16x16x128_f8f6f4 v[62:65], v[2:9], v[210:217], 0, v193, v194 op_sel_hi:[0,0,0]
	v_mfma_scale_f32_16x16x128_f8f6f4 v[58:61], v[10:17], v[210:217], 0, v193, v194 op_sel_hi:[0,0,0]
	v_mfma_scale_f32_16x16x128_f8f6f4 v[46:49], v[2:9], v[218:225], 0, v193, v194 op_sel_hi:[0,0,0]
	v_mfma_scale_f32_16x16x128_f8f6f4 v[42:45], v[10:17], v[218:225], 0, v193, v194 op_sel_hi:[0,0,0]
	s_setprio 0
	s_setprio 1
	v_mfma_scale_f32_16x16x128_f8f6f4 v[86:89], v[18:25], v[50:57], 0, v193, v194 op_sel_hi:[0,0,0]
	v_mfma_scale_f32_16x16x128_f8f6f4 v[82:85], v[26:33], v[50:57], 0, v193, v194 op_sel_hi:[0,0,0]
	v_mfma_scale_f32_16x16x128_f8f6f4 v[70:73], v[18:25], v[202:209], 0, v193, v194 op_sel_hi:[0,0,0]
	v_mfma_scale_f32_16x16x128_f8f6f4 v[66:69], v[26:33], v[202:209], 0, v193, v194 op_sel_hi:[0,0,0]
	v_mfma_scale_f32_16x16x128_f8f6f4 v[54:57], v[18:25], v[210:217], 0, v193, v194 op_sel_hi:[0,0,0]
	v_mfma_scale_f32_16x16x128_f8f6f4 v[50:53], v[26:33], v[210:217], 0, v193, v194 op_sel_hi:[0,0,0]
	v_mfma_scale_f32_16x16x128_f8f6f4 v[38:41], v[18:25], v[218:225], 0, v193, v194 op_sel_hi:[0,0,0]
	v_mfma_scale_f32_16x16x128_f8f6f4 v[34:37], v[26:33], v[218:225], 0, v193, v194 op_sel_hi:[0,0,0]
	s_setprio 0
	s_barrier
	s_add_i32 s72, 0, 0x18000
	s_add_i32 s74, 0, 0x1c000
	v_add_u32_e32 v201, s72, v171
	v_add_u32_e32 v203, s74, v171
	v_add_u32_e32 v202, s72, v182
	ds_read_b128 v[18:21], v201
	ds_read_b128 v[26:29], v201 offset:2048
	ds_read_b128 v[22:25], v202
	ds_read_b128 v[30:33], v202 offset:2048
	v_add_u32_e32 v204, s74, v182
	ds_read_b128 v[2:5], v203
	ds_read_b128 v[10:13], v203 offset:2048
	ds_read_b128 v[6:9], v204
	ds_read_b128 v[14:17], v204 offset:2048
	s_mov_b32 m0, s52
	ds_read_b128 v[206:209], v192 offset:32768
	ds_read_b128 v[210:213], v192 offset:33792
	ds_read_b128 v[214:217], v192 offset:34816
	ds_read_b128 v[218:221], v192 offset:35840
	ds_read_b128 v[222:225], v192 offset:36864
	ds_read_b128 v[226:229], v192 offset:37888
	ds_read_b128 v[230:233], v192 offset:38912
	ds_read_b128 v[234:237], v192 offset:39936
	global_load_lds_dwordx4 v172, s[24:25]
	s_mov_b32 m0, s53
	s_nop 0
	global_load_lds_dwordx4 v174, s[24:25]
	s_waitcnt vmcnt(8)
	s_waitcnt lgkmcnt(0)
	s_barrier
	s_setprio 1
	s_waitcnt lgkmcnt(0)
	v_mfma_scale_f32_16x16x128_f8f6f4 v[158:161], v[18:25], v[206:213], v[158:161], v193, v194 op_sel_hi:[0,0,0]
	v_mfma_scale_f32_16x16x128_f8f6f4 v[154:157], v[26:33], v[206:213], v[154:157], v193, v194 op_sel_hi:[0,0,0]
	v_mfma_scale_f32_16x16x128_f8f6f4 v[142:145], v[18:25], v[214:221], v[142:145], v193, v194 op_sel_hi:[0,0,0]
	v_mfma_scale_f32_16x16x128_f8f6f4 v[138:141], v[26:33], v[214:221], v[138:141], v193, v194 op_sel_hi:[0,0,0]
	v_mfma_scale_f32_16x16x128_f8f6f4 v[126:129], v[18:25], v[222:229], v[126:129], v193, v194 op_sel_hi:[0,0,0]
	v_mfma_scale_f32_16x16x128_f8f6f4 v[122:125], v[26:33], v[222:229], v[122:125], v193, v194 op_sel_hi:[0,0,0]
	v_mfma_scale_f32_16x16x128_f8f6f4 v[110:113], v[18:25], v[230:237], v[110:113], v193, v194 op_sel_hi:[0,0,0]
	v_mfma_scale_f32_16x16x128_f8f6f4 v[106:109], v[26:33], v[230:237], v[106:109], v193, v194 op_sel_hi:[0,0,0]
	s_setprio 0
	s_setprio 1
	v_mfma_scale_f32_16x16x128_f8f6f4 v[150:153], v[2:9], v[206:213], v[150:153], v193, v194 op_sel_hi:[0,0,0]
	v_mfma_scale_f32_16x16x128_f8f6f4 v[146:149], v[10:17], v[206:213], v[146:149], v193, v194 op_sel_hi:[0,0,0]
	v_mfma_scale_f32_16x16x128_f8f6f4 v[134:137], v[2:9], v[214:221], v[134:137], v193, v194 op_sel_hi:[0,0,0]
	v_mfma_scale_f32_16x16x128_f8f6f4 v[130:133], v[10:17], v[214:221], v[130:133], v193, v194 op_sel_hi:[0,0,0]
	v_mfma_scale_f32_16x16x128_f8f6f4 v[118:121], v[2:9], v[222:229], v[118:121], v193, v194 op_sel_hi:[0,0,0]
	v_mfma_scale_f32_16x16x128_f8f6f4 v[114:117], v[10:17], v[222:229], v[114:117], v193, v194 op_sel_hi:[0,0,0]
	v_mfma_scale_f32_16x16x128_f8f6f4 v[98:101], v[2:9], v[230:237], v[98:101], v193, v194 op_sel_hi:[0,0,0]
	v_mfma_scale_f32_16x16x128_f8f6f4 v[90:93], v[10:17], v[230:237], v[90:93], v193, v194 op_sel_hi:[0,0,0]
	s_setprio 0
	s_barrier
	s_add_i32 s72, s72, s48
	s_add_i32 s73, s72, 0x2000
	v_lshl_add_u64 v[176:177], v[176:177], 0, s[30:31]
	s_mov_b32 m0, s72
	s_add_u32 s6, s40, 0x4180
	ds_read_b128 v[206:209], v192 offset:49152
	ds_read_b128 v[210:213], v192 offset:50176
	ds_read_b128 v[214:217], v192 offset:51200
	ds_read_b128 v[218:221], v192 offset:52224
	ds_read_b128 v[222:225], v192 offset:53248
	ds_read_b128 v[226:229], v192 offset:54272
	ds_read_b128 v[230:233], v192 offset:55296
	ds_read_b128 v[234:237], v192 offset:56320
	global_load_lds_dwordx4 v[176:177], off
	v_lshl_add_u64 v[176:177], v[178:179], 0, s[30:31]
	s_mov_b32 m0, s73
	s_addc_u32 s7, s41, 0
	s_add_i32 s74, s74, s48
	global_load_lds_dwordx4 v[176:177], off
	v_lshl_add_u64 v[176:177], s[6:7], 0, v[166:167]
	s_mov_b32 m0, s74
	s_add_i32 s75, s74, 0x2000
	global_load_lds_dwordx4 v[176:177], off
	v_lshl_add_u64 v[176:177], s[6:7], 0, v[164:165]
	s_mov_b32 m0, s75
	s_nop 0
	global_load_lds_dwordx4 v[176:177], off
	s_mov_b32 m0, s54
	s_nop 0
	global_load_lds_dwordx4 v200, s[26:27]
	s_mov_b32 m0, s55
	s_nop 0
	global_load_lds_dwordx4 v170, s[26:27]
	s_waitcnt vmcnt(8)
	s_waitcnt lgkmcnt(0)
	s_barrier
	s_setprio 1
	s_waitcnt lgkmcnt(0)
	v_mfma_scale_f32_16x16x128_f8f6f4 v[102:105], v[18:25], v[206:213], v[102:105], v193, v194 op_sel_hi:[0,0,0]
	v_mfma_scale_f32_16x16x128_f8f6f4 v[94:97], v[26:33], v[206:213], v[94:97], v193, v194 op_sel_hi:[0,0,0]
	v_mfma_scale_f32_16x16x128_f8f6f4 v[78:81], v[18:25], v[214:221], v[78:81], v193, v194 op_sel_hi:[0,0,0]
	v_mfma_scale_f32_16x16x128_f8f6f4 v[74:77], v[26:33], v[214:221], v[74:77], v193, v194 op_sel_hi:[0,0,0]
	v_mfma_scale_f32_16x16x128_f8f6f4 v[62:65], v[18:25], v[222:229], v[62:65], v193, v194 op_sel_hi:[0,0,0]
	v_mfma_scale_f32_16x16x128_f8f6f4 v[58:61], v[26:33], v[222:229], v[58:61], v193, v194 op_sel_hi:[0,0,0]
	v_mfma_scale_f32_16x16x128_f8f6f4 v[46:49], v[18:25], v[230:237], v[46:49], v193, v194 op_sel_hi:[0,0,0]
	v_mfma_scale_f32_16x16x128_f8f6f4 v[42:45], v[26:33], v[230:237], v[42:45], v193, v194 op_sel_hi:[0,0,0]
	s_setprio 0
	s_setprio 1
	v_mfma_scale_f32_16x16x128_f8f6f4 v[86:89], v[2:9], v[206:213], v[86:89], v193, v194 op_sel_hi:[0,0,0]
	v_mfma_scale_f32_16x16x128_f8f6f4 v[82:85], v[10:17], v[206:213], v[82:85], v193, v194 op_sel_hi:[0,0,0]
	v_mfma_scale_f32_16x16x128_f8f6f4 v[70:73], v[2:9], v[214:221], v[70:73], v193, v194 op_sel_hi:[0,0,0]
	v_mfma_scale_f32_16x16x128_f8f6f4 v[66:69], v[10:17], v[214:221], v[66:69], v193, v194 op_sel_hi:[0,0,0]
	v_mfma_scale_f32_16x16x128_f8f6f4 v[54:57], v[2:9], v[222:229], v[54:57], v193, v194 op_sel_hi:[0,0,0]
	v_mfma_scale_f32_16x16x128_f8f6f4 v[50:53], v[10:17], v[222:229], v[50:53], v193, v194 op_sel_hi:[0,0,0]
	v_mfma_scale_f32_16x16x128_f8f6f4 v[38:41], v[2:9], v[230:237], v[38:41], v193, v194 op_sel_hi:[0,0,0]
	v_mfma_scale_f32_16x16x128_f8f6f4 v[34:37], v[10:17], v[230:237], v[34:37], v193, v194 op_sel_hi:[0,0,0]
	s_setprio 0
	s_barrier
	s_add_u32 s76, s40, 0x200
	v_lshl_add_u64 v[18:19], s[26:27], 0, v[174:175]
	v_lshl_add_u64 v[20:21], s[26:27], 0, v[172:173]
	s_addc_u32 s77, s41, 0
	s_mov_b64 s[6:7], 0

.LBB0_708:
	s_ashr_i32 s23, s22, 31
	ds_read_b128 v[2:5], v192
	ds_read_b128 v[10:13], v192 offset:2048
	ds_read_b128 v[6:9], v193
	ds_read_b128 v[14:17], v193 offset:2048
	ds_read_b128 v[18:21], v194
	ds_read_b128 v[26:29], v194 offset:2048
	ds_read_b128 v[22:25], v195
	ds_read_b128 v[30:33], v195 offset:2048
	s_lshl_b64 s[4:5], s[22:23], 19
	s_add_u32 s26, s38, s4
	s_addc_u32 s27, s39, s5
	s_and_b64 s[4:5], s[0:1], exec
	s_cselect_b32 s23, s27, s37
	s_cselect_b32 s64, s26, s36
	s_ashr_i32 s25, s24, 31
	s_lshl_b64 s[4:5], s[24:25], 19
	s_add_u32 s28, s40, s4
	s_addc_u32 s29, s41, s5
	s_and_b64 s[4:5], s[0:1], exec
	s_cselect_b32 s25, s29, s35
	s_cselect_b32 s65, s28, s34
	s_add_u32 s4, s36, 0x40080
	s_addc_u32 s5, s37, 0
	s_add_i32 s66, s31, 0xc000
	v_lshl_add_u64 v[34:35], s[4:5], 0, v[170:171]
	s_mov_b32 m0, s66
	s_add_i32 s67, s31, 0xe000
	ds_read_b128 v[38:41], v196
	ds_read_b128 v[42:45], v196 offset:1024
	ds_read_b128 v[46:49], v196 offset:2048
	ds_read_b128 v[50:53], v196 offset:3072
	ds_read_b128 v[54:57], v196 offset:4096
	ds_read_b128 v[58:61], v196 offset:5120
	ds_read_b128 v[62:65], v196 offset:6144
	ds_read_b128 v[66:69], v196 offset:7168
	global_load_lds_dwordx4 v[34:35], off
	v_lshl_add_u64 v[34:35], s[4:5], 0, v[166:167]
	s_mov_b32 m0, s67
	s_nop 0
	global_load_lds_dwordx4 v[34:35], off
	s_waitcnt vmcnt(8)
	s_waitcnt lgkmcnt(0)
	s_barrier
	s_setprio 1
	s_mov_b32 s4, 0
	s_mov_b32 s6, s4
	s_mov_b32 s7, s4
	s_mov_b32 s5, s4
	s_waitcnt lgkmcnt(0)
	v_mfma_scale_f32_16x16x128_f8f6f4 v[158:161], v[2:9], v[38:45], 0, v197, v198 op_sel_hi:[0,0,0]
	v_mfma_scale_f32_16x16x128_f8f6f4 v[150:153], v[10:17], v[38:45], 0, v197, v198 op_sel_hi:[0,0,0]
	v_mfma_scale_f32_16x16x128_f8f6f4 v[142:145], v[2:9], v[46:53], 0, v197, v198 op_sel_hi:[0,0,0]
	v_mfma_scale_f32_16x16x128_f8f6f4 v[134:137], v[10:17], v[46:53], 0, v197, v198 op_sel_hi:[0,0,0]
	v_mfma_scale_f32_16x16x128_f8f6f4 v[126:129], v[2:9], v[54:61], 0, v197, v198 op_sel_hi:[0,0,0]
	v_mfma_scale_f32_16x16x128_f8f6f4 v[118:121], v[10:17], v[54:61], 0, v197, v198 op_sel_hi:[0,0,0]
	v_mfma_scale_f32_16x16x128_f8f6f4 v[94:97], v[2:9], v[62:69], 0, v197, v198 op_sel_hi:[0,0,0]
	v_mfma_scale_f32_16x16x128_f8f6f4 v[78:81], v[10:17], v[62:69], 0, v197, v198 op_sel_hi:[0,0,0]
	s_setprio 0
	s_setprio 1
	v_mfma_scale_f32_16x16x128_f8f6f4 v[154:157], v[18:25], v[38:45], 0, v197, v198 op_sel_hi:[0,0,0]
	v_mfma_scale_f32_16x16x128_f8f6f4 v[146:149], v[26:33], v[38:45], 0, v197, v198 op_sel_hi:[0,0,0]
	v_mfma_scale_f32_16x16x128_f8f6f4 v[138:141], v[18:25], v[46:53], 0, v197, v198 op_sel_hi:[0,0,0]
	v_mfma_scale_f32_16x16x128_f8f6f4 v[130:133], v[26:33], v[46:53], 0, v197, v198 op_sel_hi:[0,0,0]
	v_mfma_scale_f32_16x16x128_f8f6f4 v[122:125], v[18:25], v[54:61], 0, v197, v198 op_sel_hi:[0,0,0]
	v_mfma_scale_f32_16x16x128_f8f6f4 v[110:113], v[26:33], v[54:61], 0, v197, v198 op_sel_hi:[0,0,0]
	v_mfma_scale_f32_16x16x128_f8f6f4 v[90:93], v[18:25], v[62:69], 0, v197, v198 op_sel_hi:[0,0,0]
	v_mfma_scale_f32_16x16x128_f8f6f4 v[74:77], v[26:33], v[62:69], 0, v197, v198 op_sel_hi:[0,0,0]
	s_setprio 0
	s_barrier
	s_add_i32 s5, s56, s43
	v_lshl_add_u64 v[178:179], s[34:35], 0, v[168:169]
	s_add_i32 s68, s5, 0x2000
	v_lshl_add_u64 v[38:39], v[178:179], 0, s[18:19]
	s_mov_b32 m0, s5
	v_lshl_add_u64 v[180:181], s[34:35], 0, v[164:165]
	s_add_u32 s6, s34, 0x4100
	ds_read_b128 v[200:203], v196 offset:16384
	ds_read_b128 v[204:207], v196 offset:17408
	ds_read_b128 v[208:211], v196 offset:18432
	ds_read_b128 v[212:215], v196 offset:19456
	ds_read_b128 v[216:219], v196 offset:20480
	ds_read_b128 v[220:223], v196 offset:21504
	ds_read_b128 v[224:227], v196 offset:22528
	ds_read_b128 v[228:231], v196 offset:23552
	global_load_lds_dwordx4 v[38:39], off
	v_lshl_add_u64 v[38:39], v[180:181], 0, s[18:19]
	s_mov_b32 m0, s68
	s_addc_u32 s7, s35, 0
	s_add_i32 s69, s57, s43
	global_load_lds_dwordx4 v[38:39], off
	v_lshl_add_u64 v[38:39], s[6:7], 0, v[168:169]
	s_mov_b32 m0, s69
	s_add_i32 s70, s69, 0x2000
	global_load_lds_dwordx4 v[38:39], off
	v_lshl_add_u64 v[38:39], s[6:7], 0, v[164:165]
	s_mov_b32 m0, s70
	v_lshl_add_u64 v[182:183], s[36:37], 0, v[170:171]
	global_load_lds_dwordx4 v[38:39], off
	v_lshl_add_u64 v[38:39], v[182:183], 0, s[18:19]
	s_mov_b32 m0, s31
	v_lshl_add_u64 v[184:185], s[36:37], 0, v[166:167]
	global_load_lds_dwordx4 v[38:39], off
	v_lshl_add_u64 v[38:39], v[184:185], 0, s[18:19]
	s_mov_b32 m0, s46
	s_nop 0
	global_load_lds_dwordx4 v[38:39], off
	s_waitcnt vmcnt(8)
	s_waitcnt lgkmcnt(0)
	s_barrier
	s_setprio 1
	s_waitcnt lgkmcnt(0)
	v_mfma_scale_f32_16x16x128_f8f6f4 v[114:117], v[2:9], v[200:207], 0, v197, v198 op_sel_hi:[0,0,0]
	v_mfma_scale_f32_16x16x128_f8f6f4 v[102:105], v[10:17], v[200:207], 0, v197, v198 op_sel_hi:[0,0,0]
	v_mfma_scale_f32_16x16x128_f8f6f4 v[86:89], v[2:9], v[208:215], 0, v197, v198 op_sel_hi:[0,0,0]
	v_mfma_scale_f32_16x16x128_f8f6f4 v[70:73], v[10:17], v[208:215], 0, v197, v198 op_sel_hi:[0,0,0]
	v_mfma_scale_f32_16x16x128_f8f6f4 v[62:65], v[2:9], v[216:223], 0, v197, v198 op_sel_hi:[0,0,0]
	v_mfma_scale_f32_16x16x128_f8f6f4 v[54:57], v[10:17], v[216:223], 0, v197, v198 op_sel_hi:[0,0,0]
	v_mfma_scale_f32_16x16x128_f8f6f4 v[46:49], v[2:9], v[224:231], 0, v197, v198 op_sel_hi:[0,0,0]
	v_mfma_scale_f32_16x16x128_f8f6f4 v[38:41], v[10:17], v[224:231], 0, v197, v198 op_sel_hi:[0,0,0]
	s_setprio 0
	s_setprio 1
	v_mfma_scale_f32_16x16x128_f8f6f4 v[106:109], v[18:25], v[200:207], 0, v197, v198 op_sel_hi:[0,0,0]
	v_mfma_scale_f32_16x16x128_f8f6f4 v[98:101], v[26:33], v[200:207], 0, v197, v198 op_sel_hi:[0,0,0]
	v_mfma_scale_f32_16x16x128_f8f6f4 v[82:85], v[18:25], v[208:215], 0, v197, v198 op_sel_hi:[0,0,0]
	v_mfma_scale_f32_16x16x128_f8f6f4 v[66:69], v[26:33], v[208:215], 0, v197, v198 op_sel_hi:[0,0,0]
	v_mfma_scale_f32_16x16x128_f8f6f4 v[58:61], v[18:25], v[216:223], 0, v197, v198 op_sel_hi:[0,0,0]
	v_mfma_scale_f32_16x16x128_f8f6f4 v[50:53], v[26:33], v[216:223], 0, v197, v198 op_sel_hi:[0,0,0]
	v_mfma_scale_f32_16x16x128_f8f6f4 v[42:45], v[18:25], v[224:231], 0, v197, v198 op_sel_hi:[0,0,0]
	v_mfma_scale_f32_16x16x128_f8f6f4 v[34:37], v[26:33], v[224:231], 0, v197, v198 op_sel_hi:[0,0,0]
	s_setprio 0
	s_barrier
	s_add_i32 s71, 0, 0x18000
	s_add_i32 s73, 0, 0x1c000
	v_add_u32_e32 v172, s71, v188
	v_add_u32_e32 v201, s73, v188
	v_add_u32_e32 v200, s71, v189
	ds_read_b128 v[18:21], v172
	ds_read_b128 v[26:29], v172 offset:2048
	ds_read_b128 v[22:25], v200
	ds_read_b128 v[30:33], v200 offset:2048
	v_add_u32_e32 v202, s73, v189
	ds_read_b128 v[2:5], v201
	ds_read_b128 v[10:13], v201 offset:2048
	ds_read_b128 v[6:9], v202
	ds_read_b128 v[14:17], v202 offset:2048
	s_add_u32 s6, s36, 0x40100
	s_addc_u32 s7, s37, 0
	s_mov_b32 m0, s47
	v_lshl_add_u64 v[236:237], s[6:7], 0, v[170:171]
	ds_read_b128 v[204:207], v196 offset:32768
	ds_read_b128 v[208:211], v196 offset:33792
	ds_read_b128 v[212:215], v196 offset:34816
	ds_read_b128 v[216:219], v196 offset:35840
	ds_read_b128 v[220:223], v196 offset:36864
	ds_read_b128 v[224:227], v196 offset:37888
	ds_read_b128 v[228:231], v196 offset:38912
	ds_read_b128 v[232:235], v196 offset:39936
	global_load_lds_dwordx4 v[236:237], off
	v_lshl_add_u64 v[236:237], s[6:7], 0, v[166:167]
	s_mov_b32 m0, s48
	s_nop 0
	global_load_lds_dwordx4 v[236:237], off
	s_waitcnt vmcnt(8)
	s_waitcnt lgkmcnt(0)
	s_barrier
	s_setprio 1
	s_waitcnt lgkmcnt(0)
	v_mfma_scale_f32_16x16x128_f8f6f4 v[158:161], v[18:25], v[204:211], v[158:161], v197, v198 op_sel_hi:[0,0,0]
	v_mfma_scale_f32_16x16x128_f8f6f4 v[150:153], v[26:33], v[204:211], v[150:153], v197, v198 op_sel_hi:[0,0,0]
	v_mfma_scale_f32_16x16x128_f8f6f4 v[142:145], v[18:25], v[212:219], v[142:145], v197, v198 op_sel_hi:[0,0,0]
	v_mfma_scale_f32_16x16x128_f8f6f4 v[134:137], v[26:33], v[212:219], v[134:137], v197, v198 op_sel_hi:[0,0,0]
	v_mfma_scale_f32_16x16x128_f8f6f4 v[126:129], v[18:25], v[220:227], v[126:129], v197, v198 op_sel_hi:[0,0,0]
	v_mfma_scale_f32_16x16x128_f8f6f4 v[118:121], v[26:33], v[220:227], v[118:121], v197, v198 op_sel_hi:[0,0,0]
	v_mfma_scale_f32_16x16x128_f8f6f4 v[94:97], v[18:25], v[228:235], v[94:97], v197, v198 op_sel_hi:[0,0,0]
	v_mfma_scale_f32_16x16x128_f8f6f4 v[78:81], v[26:33], v[228:235], v[78:81], v197, v198 op_sel_hi:[0,0,0]
	s_setprio 0
	s_setprio 1
	v_mfma_scale_f32_16x16x128_f8f6f4 v[154:157], v[2:9], v[204:211], v[154:157], v197, v198 op_sel_hi:[0,0,0]
	v_mfma_scale_f32_16x16x128_f8f6f4 v[146:149], v[10:17], v[204:211], v[146:149], v197, v198 op_sel_hi:[0,0,0]
	v_mfma_scale_f32_16x16x128_f8f6f4 v[138:141], v[2:9], v[212:219], v[138:141], v197, v198 op_sel_hi:[0,0,0]
	v_mfma_scale_f32_16x16x128_f8f6f4 v[130:133], v[10:17], v[212:219], v[130:133], v197, v198 op_sel_hi:[0,0,0]
	v_mfma_scale_f32_16x16x128_f8f6f4 v[122:125], v[2:9], v[220:227], v[122:125], v197, v198 op_sel_hi:[0,0,0]
	v_mfma_scale_f32_16x16x128_f8f6f4 v[110:113], v[10:17], v[220:227], v[110:113], v197, v198 op_sel_hi:[0,0,0]
	v_mfma_scale_f32_16x16x128_f8f6f4 v[90:93], v[2:9], v[228:235], v[90:93], v197, v198 op_sel_hi:[0,0,0]
	v_mfma_scale_f32_16x16x128_f8f6f4 v[74:77], v[10:17], v[228:235], v[74:77], v197, v198 op_sel_hi:[0,0,0]
	s_setprio 0
	s_barrier
	s_add_i32 s71, s71, s43
	s_add_i32 s72, s71, 0x2000
	v_lshl_add_u64 v[178:179], v[178:179], 0, s[20:21]
	s_mov_b32 m0, s71
	s_add_u32 s6, s34, 0x4180
	ds_read_b128 v[204:207], v196 offset:49152
	ds_read_b128 v[208:211], v196 offset:50176
	ds_read_b128 v[212:215], v196 offset:51200
	ds_read_b128 v[216:219], v196 offset:52224
	ds_read_b128 v[220:223], v196 offset:53248
	ds_read_b128 v[224:227], v196 offset:54272
	ds_read_b128 v[228:231], v196 offset:55296
	ds_read_b128 v[232:235], v196 offset:56320
	global_load_lds_dwordx4 v[178:179], off
	v_lshl_add_u64 v[178:179], v[180:181], 0, s[20:21]
	s_mov_b32 m0, s72
	s_addc_u32 s7, s35, 0
	s_add_i32 s73, s73, s43
	global_load_lds_dwordx4 v[178:179], off
	v_lshl_add_u64 v[178:179], s[6:7], 0, v[168:169]
	s_mov_b32 m0, s73
	s_add_i32 s74, s73, 0x2000
	global_load_lds_dwordx4 v[178:179], off
	v_lshl_add_u64 v[178:179], s[6:7], 0, v[164:165]
	s_mov_b32 m0, s74
	s_nop 0
	global_load_lds_dwordx4 v[178:179], off
	v_lshl_add_u64 v[178:179], v[182:183], 0, s[20:21]
	s_mov_b32 m0, s51
	s_nop 0
	global_load_lds_dwordx4 v[178:179], off
	v_lshl_add_u64 v[178:179], v[184:185], 0, s[20:21]
	s_mov_b32 m0, s52
	s_nop 0
	global_load_lds_dwordx4 v[178:179], off
	s_waitcnt vmcnt(8)
	s_waitcnt lgkmcnt(0)
	s_barrier
	s_setprio 1
	s_waitcnt lgkmcnt(0)
	v_mfma_scale_f32_16x16x128_f8f6f4 v[114:117], v[18:25], v[204:211], v[114:117], v197, v198 op_sel_hi:[0,0,0]
	v_mfma_scale_f32_16x16x128_f8f6f4 v[102:105], v[26:33], v[204:211], v[102:105], v197, v198 op_sel_hi:[0,0,0]
	v_mfma_scale_f32_16x16x128_f8f6f4 v[86:89], v[18:25], v[212:219], v[86:89], v197, v198 op_sel_hi:[0,0,0]
	v_mfma_scale_f32_16x16x128_f8f6f4 v[70:73], v[26:33], v[212:219], v[70:73], v197, v198 op_sel_hi:[0,0,0]
	v_mfma_scale_f32_16x16x128_f8f6f4 v[62:65], v[18:25], v[220:227], v[62:65], v197, v198 op_sel_hi:[0,0,0]
	v_mfma_scale_f32_16x16x128_f8f6f4 v[54:57], v[26:33], v[220:227], v[54:57], v197, v198 op_sel_hi:[0,0,0]
	v_mfma_scale_f32_16x16x128_f8f6f4 v[46:49], v[18:25], v[228:235], v[46:49], v197, v198 op_sel_hi:[0,0,0]
	v_mfma_scale_f32_16x16x128_f8f6f4 v[38:41], v[26:33], v[228:235], v[38:41], v197, v198 op_sel_hi:[0,0,0]
	s_setprio 0
	s_setprio 1
	v_mfma_scale_f32_16x16x128_f8f6f4 v[106:109], v[2:9], v[204:211], v[106:109], v197, v198 op_sel_hi:[0,0,0]
	v_mfma_scale_f32_16x16x128_f8f6f4 v[98:101], v[10:17], v[204:211], v[98:101], v197, v198 op_sel_hi:[0,0,0]
	v_mfma_scale_f32_16x16x128_f8f6f4 v[82:85], v[2:9], v[212:219], v[82:85], v197, v198 op_sel_hi:[0,0,0]
	v_mfma_scale_f32_16x16x128_f8f6f4 v[66:69], v[10:17], v[212:219], v[66:69], v197, v198 op_sel_hi:[0,0,0]
	v_mfma_scale_f32_16x16x128_f8f6f4 v[58:61], v[2:9], v[220:227], v[58:61], v197, v198 op_sel_hi:[0,0,0]
	v_mfma_scale_f32_16x16x128_f8f6f4 v[50:53], v[10:17], v[220:227], v[50:53], v197, v198 op_sel_hi:[0,0,0]
	v_mfma_scale_f32_16x16x128_f8f6f4 v[42:45], v[2:9], v[228:235], v[42:45], v197, v198 op_sel_hi:[0,0,0]
	v_mfma_scale_f32_16x16x128_f8f6f4 v[34:37], v[10:17], v[228:235], v[34:37], v197, v198 op_sel_hi:[0,0,0]
	s_setprio 0
	s_barrier
	s_add_u32 s75, s34, 0x200
	s_addc_u32 s76, s35, 0
	s_add_u32 s6, s36, 0x40180
	s_addc_u32 s7, s37, 0
